# v9 with the converter's fp8 weight stores as sc1 nt (write-through, not kept in L2)
# speedup vs baseline: 1.0155x; 1.0039x over previous
.Lcv_convA:
	v_mul_f32_e32 v156, 0x44000000, v2
	v_mul_f32_e32 v157, 0x44000000, v6
	v_med3_f32 v156, v156, s35, v160
	v_med3_f32 v157, v157, s35, v160
	v_cvt_pk_fp8_f32 v148, v156, v157
	v_mul_f32_e32 v158, 0x44000000, v10
	v_mul_f32_e32 v159, 0x44000000, v14
	v_med3_f32 v158, v158, s35, v160
	v_med3_f32 v159, v159, s35, v160
	v_cvt_pk_fp8_f32 v148, v158, v159 op_sel:[0,0,1]
	v_mul_f32_e32 v156, 0x44000000, v18
	v_mul_f32_e32 v157, 0x44000000, v22
	v_med3_f32 v156, v156, s35, v160
	v_med3_f32 v157, v157, s35, v160
	v_cvt_pk_fp8_f32 v149, v156, v157
	v_mul_f32_e32 v158, 0x44000000, v26
	v_mul_f32_e32 v159, 0x44000000, v30
	v_med3_f32 v158, v158, s35, v160
	v_med3_f32 v159, v159, s35, v160
	v_cvt_pk_fp8_f32 v149, v158, v159 op_sel:[0,0,1]
	v_mul_f32_e32 v156, 0x44000000, v3
	v_mul_f32_e32 v157, 0x44000000, v7
	v_med3_f32 v156, v156, s35, v160
	v_med3_f32 v157, v157, s35, v160
	v_cvt_pk_fp8_f32 v150, v156, v157
	v_mul_f32_e32 v158, 0x44000000, v11
	v_mul_f32_e32 v159, 0x44000000, v15
	v_med3_f32 v158, v158, s35, v160
	v_med3_f32 v159, v159, s35, v160
	v_cvt_pk_fp8_f32 v150, v158, v159 op_sel:[0,0,1]
	v_mul_f32_e32 v156, 0x44000000, v19
	v_mul_f32_e32 v157, 0x44000000, v23
	v_med3_f32 v156, v156, s35, v160
	v_med3_f32 v157, v157, s35, v160
	v_cvt_pk_fp8_f32 v151, v156, v157
	v_mul_f32_e32 v158, 0x44000000, v27
	v_mul_f32_e32 v159, 0x44000000, v31
	v_med3_f32 v158, v158, s35, v160
	v_med3_f32 v159, v159, s35, v160
	v_cvt_pk_fp8_f32 v151, v158, v159 op_sel:[0,0,1]
	v_mul_f32_e32 v156, 0x44000000, v4
	v_mul_f32_e32 v157, 0x44000000, v8
	v_med3_f32 v156, v156, s35, v160
	v_med3_f32 v157, v157, s35, v160
	v_cvt_pk_fp8_f32 v152, v156, v157
	v_mul_f32_e32 v158, 0x44000000, v12
	v_mul_f32_e32 v159, 0x44000000, v16
	v_med3_f32 v158, v158, s35, v160
	v_med3_f32 v159, v159, s35, v160
	v_cvt_pk_fp8_f32 v152, v158, v159 op_sel:[0,0,1]
	ds_write2_b64 v71, v[148:149], v[150:151] offset0:0 offset1:16
	v_mul_f32_e32 v156, 0x44000000, v20
	v_mul_f32_e32 v157, 0x44000000, v24
	v_med3_f32 v156, v156, s35, v160
	v_med3_f32 v157, v157, s35, v160
	v_cvt_pk_fp8_f32 v153, v156, v157
	v_mul_f32_e32 v158, 0x44000000, v28
	v_mul_f32_e32 v159, 0x44000000, v32
	v_med3_f32 v158, v158, s35, v160
	v_med3_f32 v159, v159, s35, v160
	v_cvt_pk_fp8_f32 v153, v158, v159 op_sel:[0,0,1]
	v_mul_f32_e32 v156, 0x44000000, v5
	v_mul_f32_e32 v157, 0x44000000, v9
	v_med3_f32 v156, v156, s35, v160
	v_med3_f32 v157, v157, s35, v160
	v_cvt_pk_fp8_f32 v154, v156, v157
	v_mul_f32_e32 v158, 0x44000000, v13
	v_mul_f32_e32 v159, 0x44000000, v17
	v_med3_f32 v158, v158, s35, v160
	v_med3_f32 v159, v159, s35, v160
	v_cvt_pk_fp8_f32 v154, v158, v159 op_sel:[0,0,1]
	v_mul_f32_e32 v156, 0x44000000, v21
	v_mul_f32_e32 v157, 0x44000000, v25
	v_med3_f32 v156, v156, s35, v160
	v_med3_f32 v157, v157, s35, v160
	v_cvt_pk_fp8_f32 v155, v156, v157
	v_mul_f32_e32 v158, 0x44000000, v29
	v_mul_f32_e32 v159, 0x44000000, v33
	v_med3_f32 v158, v158, s35, v160
	v_med3_f32 v159, v159, s35, v160
	v_cvt_pk_fp8_f32 v155, v158, v159 op_sel:[0,0,1]
	v_mul_f32_e32 v156, 0x44000000, v34
	v_mul_f32_e32 v157, 0x44000000, v38
	v_med3_f32 v156, v156, s35, v160
	v_med3_f32 v157, v157, s35, v160
	v_cvt_pk_fp8_f32 v148, v156, v157
	v_mul_f32_e32 v158, 0x44000000, v42
	v_mul_f32_e32 v159, 0x44000000, v46
	v_med3_f32 v158, v158, s35, v160
	v_med3_f32 v159, v159, s35, v160
	v_cvt_pk_fp8_f32 v148, v158, v159 op_sel:[0,0,1]
	ds_write2_b64 v71, v[152:153], v[154:155] offset0:32 offset1:48
	v_mul_f32_e32 v156, 0x44000000, v50
	v_mul_f32_e32 v157, 0x44000000, v54
	v_med3_f32 v156, v156, s35, v160
	v_med3_f32 v157, v157, s35, v160
	v_cvt_pk_fp8_f32 v149, v156, v157
	v_mul_f32_e32 v158, 0x44000000, v58
	v_mul_f32_e32 v159, 0x44000000, v62
	v_med3_f32 v158, v158, s35, v160
	v_med3_f32 v159, v159, s35, v160
	v_cvt_pk_fp8_f32 v149, v158, v159 op_sel:[0,0,1]
	v_mul_f32_e32 v156, 0x44000000, v35
	v_mul_f32_e32 v157, 0x44000000, v39
	v_med3_f32 v156, v156, s35, v160
	v_med3_f32 v157, v157, s35, v160
	v_cvt_pk_fp8_f32 v150, v156, v157
	v_mul_f32_e32 v158, 0x44000000, v43
	v_mul_f32_e32 v159, 0x44000000, v47
	v_med3_f32 v158, v158, s35, v160
	v_med3_f32 v159, v159, s35, v160
	v_cvt_pk_fp8_f32 v150, v158, v159 op_sel:[0,0,1]
	v_mul_f32_e32 v156, 0x44000000, v51
	v_mul_f32_e32 v157, 0x44000000, v55
	v_med3_f32 v156, v156, s35, v160
	v_med3_f32 v157, v157, s35, v160
	v_cvt_pk_fp8_f32 v151, v156, v157
	v_mul_f32_e32 v158, 0x44000000, v59
	v_mul_f32_e32 v159, 0x44000000, v63
	v_med3_f32 v158, v158, s35, v160
	v_med3_f32 v159, v159, s35, v160
	v_cvt_pk_fp8_f32 v151, v158, v159 op_sel:[0,0,1]
	v_mul_f32_e32 v156, 0x44000000, v36
	v_mul_f32_e32 v157, 0x44000000, v40
	v_med3_f32 v156, v156, s35, v160
	v_med3_f32 v157, v157, s35, v160
	v_cvt_pk_fp8_f32 v152, v156, v157
	v_mul_f32_e32 v158, 0x44000000, v44
	v_mul_f32_e32 v159, 0x44000000, v48
	v_med3_f32 v158, v158, s35, v160
	v_med3_f32 v159, v159, s35, v160
	v_cvt_pk_fp8_f32 v152, v158, v159 op_sel:[0,0,1]
	ds_write2_b64 v72, v[148:149], v[150:151] offset0:0 offset1:16
	v_mul_f32_e32 v156, 0x44000000, v52
	v_mul_f32_e32 v157, 0x44000000, v56
	v_med3_f32 v156, v156, s35, v160
	v_med3_f32 v157, v157, s35, v160
	v_cvt_pk_fp8_f32 v153, v156, v157
	v_mul_f32_e32 v158, 0x44000000, v60
	v_mul_f32_e32 v159, 0x44000000, v64
	v_med3_f32 v158, v158, s35, v160
	v_med3_f32 v159, v159, s35, v160
	v_cvt_pk_fp8_f32 v153, v158, v159 op_sel:[0,0,1]
	v_mul_f32_e32 v156, 0x44000000, v37
	v_mul_f32_e32 v157, 0x44000000, v41
	v_med3_f32 v156, v156, s35, v160
	v_med3_f32 v157, v157, s35, v160
	v_cvt_pk_fp8_f32 v154, v156, v157
	v_mul_f32_e32 v158, 0x44000000, v45
	v_mul_f32_e32 v159, 0x44000000, v49
	v_med3_f32 v158, v158, s35, v160
	v_med3_f32 v159, v159, s35, v160
	v_cvt_pk_fp8_f32 v154, v158, v159 op_sel:[0,0,1]
	v_mul_f32_e32 v156, 0x44000000, v53
	v_mul_f32_e32 v157, 0x44000000, v57
	v_med3_f32 v156, v156, s35, v160
	v_med3_f32 v157, v157, s35, v160
	v_cvt_pk_fp8_f32 v155, v156, v157
	v_mul_f32_e32 v158, 0x44000000, v61
	v_mul_f32_e32 v159, 0x44000000, v65
	v_med3_f32 v158, v158, s35, v160
	v_med3_f32 v159, v159, s35, v160
	v_cvt_pk_fp8_f32 v155, v158, v159 op_sel:[0,0,1]
	s_nop 0
	ds_write2_b64 v72, v[152:153], v[154:155] offset0:32 offset1:48
	s_waitcnt lgkmcnt(0)
	s_barrier
	ds_read_b128 v[236:239], v75 offset:0
	ds_read_b128 v[240:243], v75 offset:8192
	ds_read_b128 v[244:247], v75 offset:16384
	ds_read_b128 v[248:251], v75 offset:24576
	s_mov_b64 s[68:69], s[52:53]
	s_waitcnt lgkmcnt(3)
	global_store_dwordx4 v76, v[236:239], s[68:69] sc1 nt
	s_add_u32 s68, s68, 0x20000
	s_addc_u32 s69, s69, 0
	s_waitcnt lgkmcnt(2)
	global_store_dwordx4 v76, v[240:243], s[68:69] sc1 nt
	s_add_u32 s68, s68, s86
	s_addc_u32 s69, s69, 0
	s_waitcnt lgkmcnt(1)
	global_store_dwordx4 v76, v[244:247], s[68:69] sc1 nt
	s_add_u32 s68, s68, 0x20000
	s_addc_u32 s69, s69, 0
	s_waitcnt lgkmcnt(0)
	global_store_dwordx4 v76, v[248:251], s[68:69] sc1 nt
	s_sub_u32 s41, s41, 1
	s_cmp_eq_u32 s41, 0
	s_cbranch_scc1 .Lcv_done
	s_min_u32 s0, s30, 0x2fff
	s_add_u32 s30, s30, s31
	s_cmp_lt_u32 s0, 0x2000
	s_cbranch_scc0 .Lcv_w2_3
	s_lshr_b32 s1, s0, 8
	s_bfe_u32 s3, s0, 0x40004
	s_bfe_u32 s7, s0, 0x30001
	s_and_b32 s0, s0, 1
	s_lshl_b32 s6, s1, 25
	s_lshl_b32 s49, s3, 21
	s_add_u32 s6, s6, s49
	s_lshl_b32 s49, s34, 17
	s_add_u32 s6, s6, s49
	s_lshl_b32 s49, s0, 13
	s_add_u32 s6, s6, s49
	s_lshl_b32 s49, s7, 10
	s_add_u32 s6, s6, s49
	s_add_u32 s62, s8, s6
	s_addc_u32 s63, s9, 0
	s_lshl_b32 s6, s1, 23
	s_lshl_b32 s49, s7, 20
	s_add_u32 s6, s6, s49
	s_lshl_b32 s49, s0, 18
	s_add_u32 s6, s6, s49
	s_lshl_b32 s49, s3, 7
	s_add_u32 s6, s6, s49
	s_add_u32 s52, s12, s6
	s_addc_u32 s53, s13, 0
	s_mov_b32 s70, 0x4000
	s_mov_b32 s71, 0xe4000
	s_mov_b32 s86, 0x60000
	v_mov_b32_e32 v70, v68
	s_branch .Lcv_dec_done_3

.Lcv_loopB:
	s_waitcnt vmcnt(20)
	v_mul_f32_e32 v156, 0x44000000, v84
	v_mul_f32_e32 v157, 0x44000000, v88
	v_med3_f32 v156, v156, s35, v160
	v_med3_f32 v157, v157, s35, v160
	v_cvt_pk_fp8_f32 v148, v156, v157
	v_mul_f32_e32 v158, 0x44000000, v92
	v_mul_f32_e32 v159, 0x44000000, v96
	v_med3_f32 v158, v158, s35, v160
	v_med3_f32 v159, v159, s35, v160
	v_cvt_pk_fp8_f32 v148, v158, v159 op_sel:[0,0,1]
	v_mul_f32_e32 v156, 0x44000000, v100
	v_mul_f32_e32 v157, 0x44000000, v104
	v_med3_f32 v156, v156, s35, v160
	v_med3_f32 v157, v157, s35, v160
	v_cvt_pk_fp8_f32 v149, v156, v157
	v_mul_f32_e32 v158, 0x44000000, v108
	v_mul_f32_e32 v159, 0x44000000, v112
	v_med3_f32 v158, v158, s35, v160
	v_med3_f32 v159, v159, s35, v160
	v_cvt_pk_fp8_f32 v149, v158, v159 op_sel:[0,0,1]
	v_mul_f32_e32 v156, 0x44000000, v85
	v_mul_f32_e32 v157, 0x44000000, v89
	v_med3_f32 v156, v156, s35, v160
	v_med3_f32 v157, v157, s35, v160
	v_cvt_pk_fp8_f32 v150, v156, v157
	v_mul_f32_e32 v158, 0x44000000, v93
	v_mul_f32_e32 v159, 0x44000000, v97
	v_med3_f32 v158, v158, s35, v160
	v_med3_f32 v159, v159, s35, v160
	v_cvt_pk_fp8_f32 v150, v158, v159 op_sel:[0,0,1]
	v_mul_f32_e32 v156, 0x44000000, v101
	v_mul_f32_e32 v157, 0x44000000, v105
	v_med3_f32 v156, v156, s35, v160
	v_med3_f32 v157, v157, s35, v160
	v_cvt_pk_fp8_f32 v151, v156, v157
	v_mul_f32_e32 v158, 0x44000000, v109
	v_mul_f32_e32 v159, 0x44000000, v113
	v_med3_f32 v158, v158, s35, v160
	v_med3_f32 v159, v159, s35, v160
	v_cvt_pk_fp8_f32 v151, v158, v159 op_sel:[0,0,1]
	v_mul_f32_e32 v156, 0x44000000, v86
	v_mul_f32_e32 v157, 0x44000000, v90
	v_med3_f32 v156, v156, s35, v160
	v_med3_f32 v157, v157, s35, v160
	v_cvt_pk_fp8_f32 v152, v156, v157
	v_mul_f32_e32 v158, 0x44000000, v94
	v_mul_f32_e32 v159, 0x44000000, v98
	v_med3_f32 v158, v158, s35, v160
	v_med3_f32 v159, v159, s35, v160
	v_cvt_pk_fp8_f32 v152, v158, v159 op_sel:[0,0,1]
	ds_write2_b64 v73, v[148:149], v[150:151] offset0:0 offset1:16
	v_mul_f32_e32 v156, 0x44000000, v102
	v_mul_f32_e32 v157, 0x44000000, v106
	v_med3_f32 v156, v156, s35, v160
	v_med3_f32 v157, v157, s35, v160
	v_cvt_pk_fp8_f32 v153, v156, v157
	v_mul_f32_e32 v158, 0x44000000, v110
	v_mul_f32_e32 v159, 0x44000000, v114
	v_med3_f32 v158, v158, s35, v160
	v_med3_f32 v159, v159, s35, v160
	v_cvt_pk_fp8_f32 v153, v158, v159 op_sel:[0,0,1]
	v_mul_f32_e32 v156, 0x44000000, v87
	v_mul_f32_e32 v157, 0x44000000, v91
	v_med3_f32 v156, v156, s35, v160
	v_med3_f32 v157, v157, s35, v160
	v_cvt_pk_fp8_f32 v154, v156, v157
	v_mul_f32_e32 v158, 0x44000000, v95
	v_mul_f32_e32 v159, 0x44000000, v99
	v_med3_f32 v158, v158, s35, v160
	v_med3_f32 v159, v159, s35, v160
	v_cvt_pk_fp8_f32 v154, v158, v159 op_sel:[0,0,1]
	v_mul_f32_e32 v156, 0x44000000, v103
	v_mul_f32_e32 v157, 0x44000000, v107
	v_med3_f32 v156, v156, s35, v160
	v_med3_f32 v157, v157, s35, v160
	v_cvt_pk_fp8_f32 v155, v156, v157
	v_mul_f32_e32 v158, 0x44000000, v111
	v_mul_f32_e32 v159, 0x44000000, v115
	v_med3_f32 v158, v158, s35, v160
	v_med3_f32 v159, v159, s35, v160
	v_cvt_pk_fp8_f32 v155, v158, v159 op_sel:[0,0,1]
	v_mul_f32_e32 v156, 0x44000000, v116
	v_mul_f32_e32 v157, 0x44000000, v120
	v_med3_f32 v156, v156, s35, v160
	v_med3_f32 v157, v157, s35, v160
	v_cvt_pk_fp8_f32 v148, v156, v157
	v_mul_f32_e32 v158, 0x44000000, v124
	v_mul_f32_e32 v159, 0x44000000, v128
	v_med3_f32 v158, v158, s35, v160
	v_med3_f32 v159, v159, s35, v160
	v_cvt_pk_fp8_f32 v148, v158, v159 op_sel:[0,0,1]
	ds_write2_b64 v73, v[152:153], v[154:155] offset0:32 offset1:48
	v_mul_f32_e32 v156, 0x44000000, v132
	v_mul_f32_e32 v157, 0x44000000, v136
	v_med3_f32 v156, v156, s35, v160
	v_med3_f32 v157, v157, s35, v160
	v_cvt_pk_fp8_f32 v149, v156, v157
	v_mul_f32_e32 v158, 0x44000000, v140
	v_mul_f32_e32 v159, 0x44000000, v144
	v_med3_f32 v158, v158, s35, v160
	v_med3_f32 v159, v159, s35, v160
	v_cvt_pk_fp8_f32 v149, v158, v159 op_sel:[0,0,1]
	v_mul_f32_e32 v156, 0x44000000, v117
	v_mul_f32_e32 v157, 0x44000000, v121
	v_med3_f32 v156, v156, s35, v160
	v_med3_f32 v157, v157, s35, v160
	v_cvt_pk_fp8_f32 v150, v156, v157
	v_mul_f32_e32 v158, 0x44000000, v125
	v_mul_f32_e32 v159, 0x44000000, v129
	v_med3_f32 v158, v158, s35, v160
	v_med3_f32 v159, v159, s35, v160
	v_cvt_pk_fp8_f32 v150, v158, v159 op_sel:[0,0,1]
	v_mul_f32_e32 v156, 0x44000000, v133
	v_mul_f32_e32 v157, 0x44000000, v137
	v_med3_f32 v156, v156, s35, v160
	v_med3_f32 v157, v157, s35, v160
	v_cvt_pk_fp8_f32 v151, v156, v157
	v_mul_f32_e32 v158, 0x44000000, v141
	v_mul_f32_e32 v159, 0x44000000, v145
	v_med3_f32 v158, v158, s35, v160
	v_med3_f32 v159, v159, s35, v160
	v_cvt_pk_fp8_f32 v151, v158, v159 op_sel:[0,0,1]
	v_mul_f32_e32 v156, 0x44000000, v118
	v_mul_f32_e32 v157, 0x44000000, v122
	v_med3_f32 v156, v156, s35, v160
	v_med3_f32 v157, v157, s35, v160
	v_cvt_pk_fp8_f32 v152, v156, v157
	v_mul_f32_e32 v158, 0x44000000, v126
	v_mul_f32_e32 v159, 0x44000000, v130
	v_med3_f32 v158, v158, s35, v160
	v_med3_f32 v159, v159, s35, v160
	v_cvt_pk_fp8_f32 v152, v158, v159 op_sel:[0,0,1]
	ds_write2_b64 v74, v[148:149], v[150:151] offset0:0 offset1:16
	v_mul_f32_e32 v156, 0x44000000, v134
	v_mul_f32_e32 v157, 0x44000000, v138
	v_med3_f32 v156, v156, s35, v160
	v_med3_f32 v157, v157, s35, v160
	v_cvt_pk_fp8_f32 v153, v156, v157
	v_mul_f32_e32 v158, 0x44000000, v142
	v_mul_f32_e32 v159, 0x44000000, v146
	v_med3_f32 v158, v158, s35, v160
	v_med3_f32 v159, v159, s35, v160
	v_cvt_pk_fp8_f32 v153, v158, v159 op_sel:[0,0,1]
	v_mul_f32_e32 v156, 0x44000000, v119
	v_mul_f32_e32 v157, 0x44000000, v123
	v_med3_f32 v156, v156, s35, v160
	v_med3_f32 v157, v157, s35, v160
	v_cvt_pk_fp8_f32 v154, v156, v157
	v_mul_f32_e32 v158, 0x44000000, v127
	v_mul_f32_e32 v159, 0x44000000, v131
	v_med3_f32 v158, v158, s35, v160
	v_med3_f32 v159, v159, s35, v160
	v_cvt_pk_fp8_f32 v154, v158, v159 op_sel:[0,0,1]
	v_mul_f32_e32 v156, 0x44000000, v135
	v_mul_f32_e32 v157, 0x44000000, v139
	v_med3_f32 v156, v156, s35, v160
	v_med3_f32 v157, v157, s35, v160
	v_cvt_pk_fp8_f32 v155, v156, v157
	v_mul_f32_e32 v158, 0x44000000, v143
	v_mul_f32_e32 v159, 0x44000000, v147
	v_med3_f32 v158, v158, s35, v160
	v_med3_f32 v159, v159, s35, v160
	v_cvt_pk_fp8_f32 v155, v158, v159 op_sel:[0,0,1]
	s_nop 0
	ds_write2_b64 v74, v[152:153], v[154:155] offset0:32 offset1:48
	s_waitcnt lgkmcnt(0)
	s_barrier
	ds_read_b128 v[236:239], v75 offset:32768
	ds_read_b128 v[240:243], v75 offset:40960
	ds_read_b128 v[244:247], v75 offset:49152
	ds_read_b128 v[248:251], v75 offset:57344
	s_mov_b64 s[68:69], s[58:59]
	s_waitcnt lgkmcnt(3)
	global_store_dwordx4 v76, v[236:239], s[68:69] sc1 nt
	s_add_u32 s68, s68, 0x20000
	s_addc_u32 s69, s69, 0
	s_waitcnt lgkmcnt(2)
	global_store_dwordx4 v76, v[240:243], s[68:69] sc1 nt
	s_add_u32 s68, s68, s87
	s_addc_u32 s69, s69, 0
	s_waitcnt lgkmcnt(1)
	global_store_dwordx4 v76, v[244:247], s[68:69] sc1 nt
	s_add_u32 s68, s68, 0x20000
	s_addc_u32 s69, s69, 0
	s_waitcnt lgkmcnt(0)
	global_store_dwordx4 v76, v[248:251], s[68:69] sc1 nt
	s_sub_u32 s41, s41, 1
	s_cmp_eq_u32 s41, 0
	s_cbranch_scc1 .Lcv_done
	s_min_u32 s0, s30, 0x2fff
	s_add_u32 s30, s30, s31
	s_cmp_lt_u32 s0, 0x2000
	s_cbranch_scc0 .Lcv_w2_4
	s_lshr_b32 s1, s0, 8
	s_bfe_u32 s3, s0, 0x40004
	s_bfe_u32 s7, s0, 0x30001
	s_and_b32 s0, s0, 1
	s_lshl_b32 s6, s1, 25
	s_lshl_b32 s49, s3, 21
	s_add_u32 s6, s6, s49
	s_lshl_b32 s49, s34, 17
	s_add_u32 s6, s6, s49
	s_lshl_b32 s49, s0, 13
	s_add_u32 s6, s6, s49
	s_lshl_b32 s49, s7, 10
	s_add_u32 s6, s6, s49
	s_add_u32 s62, s8, s6
	s_addc_u32 s63, s9, 0
	s_lshl_b32 s6, s1, 23
	s_lshl_b32 s49, s7, 20
	s_add_u32 s6, s6, s49
	s_lshl_b32 s49, s0, 18
	s_add_u32 s6, s6, s49
	s_lshl_b32 s49, s3, 7
	s_add_u32 s6, s6, s49
	s_add_u32 s58, s12, s6
	s_addc_u32 s59, s13, 0
	s_mov_b32 s70, 0x4000
	s_mov_b32 s71, 0xe4000
	s_mov_b32 s87, 0x60000
	v_mov_b32_e32 v70, v68
	s_branch .Lcv_dec_done_4
